# nt hint on the combine phase's read-once expert-output (Y) loads
# speedup vs baseline: 1.0739x; 1.0013x over previous
.LBB0_1731:
	s_add_u32 s0, s84, s6
	s_addc_u32 s1, s85, s7
	s_add_u32 s8, s0, 0x2bc10000
	s_addc_u32 s9, s1, 0
	v_mov_b32_e32 v11, 0x2bc10000
	global_load_dwordx4 v[2:5], v35, s[8:9] offset:16
	global_load_dwordx4 v[36:39], v11, s[0:1]
	v_lshl_add_u64 v[30:31], s[84:85], 0, v[28:29]
	s_mov_b32 s0, 0x178000
	v_add_co_u32_e32 v32, vcc, s0, v30
	v_lshlrev_b32_e32 v11, 1, v10
	s_nop 0
	v_addc_co_u32_e32 v33, vcc, 0, v31, vcc
	global_load_dwordx2 v[40:41], v[32:33], off
	v_lshlrev_b32_e32 v34, 2, v6
	v_lshlrev_b32_e32 v13, 2, v12
	v_lshlrev_b32_e32 v15, 2, v10
	s_waitcnt vmcnt(0)
	v_lshlrev_b32_e32 v76, 16, v40
	v_and_b32_e32 v77, 0xffff0000, v40
	v_lshlrev_b32_e32 v74, 16, v41
	v_and_b32_e32 v75, 0xffff0000, v41
	v_ashrrev_i32_e32 v41, 31, v36
	v_mov_b32_e32 v40, v36
	v_lshlrev_b64 v[40:41], 11, v[40:41]
	v_lshl_add_u64 v[42:43], v[8:9], 0, v[40:41]
	global_load_dwordx2 v[114:115], v[42:43], off
	v_ashrrev_i32_e32 v43, 31, v37
	v_mov_b32_e32 v42, v37
	v_lshlrev_b64 v[36:37], 11, v[42:43]
	v_lshl_add_u64 v[42:43], v[8:9], 0, v[36:37]
	global_load_dwordx2 v[116:117], v[42:43], off
	v_ashrrev_i32_e32 v43, 31, v38
	v_mov_b32_e32 v42, v38
	v_lshlrev_b64 v[42:43], 11, v[42:43]
	v_lshl_add_u64 v[44:45], v[8:9], 0, v[42:43]
	global_load_dwordx2 v[118:119], v[44:45], off
	v_ashrrev_i32_e32 v45, 31, v39
	v_mov_b32_e32 v44, v39
	v_lshl_add_u64 v[36:37], s[4:5], 0, v[36:37]
	v_lshlrev_b64 v[38:39], 11, v[44:45]
	v_readfirstlane_b32 s10, v36
	v_readfirstlane_b32 s11, v37
	v_lshl_add_u64 v[36:37], s[4:5], 0, v[42:43]
	v_lshl_add_u64 v[40:41], s[4:5], 0, v[40:41]
	v_readfirstlane_b32 s14, v36
	v_readfirstlane_b32 s15, v37
	v_lshl_add_u64 v[36:37], s[4:5], 0, v[38:39]
	v_lshl_add_u64 v[44:45], v[8:9], 0, v[38:39]
	v_readfirstlane_b32 s8, v40
	v_readfirstlane_b32 s9, v41
	v_readfirstlane_b32 s16, v36
	v_readfirstlane_b32 s17, v37
	global_load_dwordx2 v[120:121], v[44:45], off
	s_nop 0
	global_load_dwordx2 v[44:45], v[32:33], off offset:512
	global_load_dwordx2 v[106:107], v11, s[8:9] nt
	global_load_dwordx2 v[108:109], v11, s[10:11] nt
	global_load_dwordx2 v[110:111], v11, s[14:15] nt
	global_load_dwordx2 v[112:113], v11, s[16:17] nt
	global_load_dwordx2 v[36:37], v[32:33], off offset:1024
	s_waitcnt vmcnt(0)
	v_lshlrev_b32_e32 v122, 16, v120
	v_lshlrev_b32_e32 v80, 16, v44
	v_and_b32_e32 v81, 0xffff0000, v44
	v_lshlrev_b32_e32 v78, 16, v45
	v_and_b32_e32 v79, 0xffff0000, v45
	v_lshlrev_b32_e32 v84, 16, v36
	v_and_b32_e32 v85, 0xffff0000, v36
	v_lshlrev_b32_e32 v82, 16, v37
	v_and_b32_e32 v83, 0xffff0000, v37
	global_load_dwordx2 v[104:105], v1, s[8:9] nt
	global_load_dwordx2 v[102:103], v1, s[10:11] nt
	global_load_dwordx2 v[100:101], v1, s[14:15] nt
	global_load_dwordx2 v[90:91], v1, s[16:17] nt
	global_load_dwordx2 v[36:37], v[32:33], off offset:1536
	global_load_dwordx2 v[98:99], v7, s[8:9] nt
	global_load_dwordx2 v[96:97], v7, s[10:11] nt
	global_load_dwordx2 v[94:95], v7, s[14:15] nt
	global_load_dwordx2 v[92:93], v7, s[16:17] nt
	global_load_dwordx2 v[66:67], v[32:33], off offset:2048
	v_and_b32_e32 v123, 0xffff0000, v120
	s_waitcnt vmcnt(0)
	v_lshlrev_b32_e32 v86, 16, v36
	v_and_b32_e32 v87, 0xffff0000, v36
	v_lshlrev_b32_e32 v88, 16, v37
	v_and_b32_e32 v89, 0xffff0000, v37
	v_ashrrev_i32_e32 v37, 31, v2
	v_mov_b32_e32 v36, v2
	v_lshlrev_b64 v[36:37], 11, v[36:37]
	v_lshl_add_u64 v[38:39], v[8:9], 0, v[36:37]
	global_load_dwordx2 v[58:59], v[38:39], off
	v_ashrrev_i32_e32 v39, 31, v3
	v_mov_b32_e32 v38, v3
	v_lshlrev_b64 v[2:3], 11, v[38:39]
	v_lshl_add_u64 v[38:39], v[8:9], 0, v[2:3]
	global_load_dwordx2 v[60:61], v[38:39], off
	v_ashrrev_i32_e32 v39, 31, v4
	v_mov_b32_e32 v38, v4
	v_lshlrev_b64 v[38:39], 11, v[38:39]
	v_lshl_add_u64 v[40:41], v[8:9], 0, v[38:39]
	global_load_dwordx2 v[62:63], v[40:41], off
	v_ashrrev_i32_e32 v41, 31, v5
	v_mov_b32_e32 v40, v5
	v_lshl_add_u64 v[2:3], s[4:5], 0, v[2:3]
	v_lshlrev_b64 v[4:5], 11, v[40:41]
	v_readfirstlane_b32 s8, v2
	v_readfirstlane_b32 s9, v3
	v_lshl_add_u64 v[2:3], s[4:5], 0, v[38:39]
	v_lshl_add_u64 v[36:37], s[4:5], 0, v[36:37]
	v_readfirstlane_b32 s10, v2
	v_readfirstlane_b32 s11, v3
	v_lshl_add_u64 v[2:3], s[4:5], 0, v[4:5]
	v_lshl_add_u64 v[40:41], v[8:9], 0, v[4:5]
	v_readfirstlane_b32 s0, v36
	v_readfirstlane_b32 s1, v37
	v_readfirstlane_b32 s14, v2
	v_readfirstlane_b32 s15, v3
	global_load_dwordx2 v[64:65], v[40:41], off
	global_load_dwordx2 v[68:69], v[32:33], off offset:2560
	global_load_dwordx2 v[52:53], v11, s[8:9] nt
	global_load_dwordx2 v[50:51], v11, s[0:1] nt
	global_load_dwordx2 v[54:55], v11, s[10:11] nt
	global_load_dwordx2 v[56:57], v11, s[14:15] nt
	global_load_dwordx2 v[70:71], v[32:33], off offset:3072
	global_load_dwordx2 v[48:49], v1, s[0:1] nt
	global_load_dwordx2 v[46:47], v1, s[8:9] nt
	global_load_dwordx2 v[44:45], v1, s[10:11] nt
	global_load_dwordx2 v[42:43], v1, s[14:15] nt
	global_load_dwordx2 v[72:73], v[32:33], off offset:3584
	global_load_dwordx2 v[40:41], v7, s[0:1] nt
	global_load_dwordx2 v[38:39], v7, s[8:9] nt
	global_load_dwordx2 v[36:37], v7, s[10:11] nt
	s_nop 0
	global_load_dwordx2 v[32:33], v7, s[14:15] nt
	s_ashr_i32 s0, s2, 31
	s_lshr_b32 s0, s0, 20
	s_add_i32 s0, s2, s0
	s_ashr_i32 s0, s0, 12
	s_cmpk_lt_i32 s2, 0x4000
	v_lshlrev_b32_e32 v2, 16, v114
	v_and_b32_e32 v3, 0xffff0000, v114
	v_lshlrev_b32_e32 v4, 16, v116
	v_and_b32_e32 v5, 0xffff0000, v116
	s_cselect_b32 s0, s0, 4
	v_pk_add_f32 v[2:3], v[2:3], v[4:5]
	v_lshlrev_b32_e32 v4, 16, v118
	v_and_b32_e32 v5, 0xffff0000, v118
	s_mul_i32 s10, s0, 0x6000
	v_pk_add_f32 v[4:5], v[4:5], v[122:123]
	s_mul_hi_i32 s3, s0, 0x6000
	s_add_u32 s8, s18, s10
	v_pk_add_f32 v[2:3], v[2:3], v[4:5]
	v_lshlrev_b32_e32 v4, 16, v115
	v_and_b32_e32 v5, 0xffff0000, v115
	v_lshlrev_b32_e32 v114, 16, v117
	v_and_b32_e32 v115, 0xffff0000, v117
	s_addc_u32 s9, s19, s3
	v_pk_add_f32 v[4:5], v[4:5], v[114:115]
	v_lshlrev_b32_e32 v114, 16, v119
	v_and_b32_e32 v115, 0xffff0000, v119
	v_lshlrev_b32_e32 v116, 16, v121
	v_and_b32_e32 v117, 0xffff0000, v121
	v_pk_add_f32 v[114:115], v[114:115], v[116:117]
	v_lshl_add_u64 v[116:117], s[8:9], 0, v[34:35]
	s_mov_b64 s[0:1], 0x5000
	v_pk_add_f32 v[4:5], v[4:5], v[114:115]
	v_lshl_add_u64 v[114:115], v[116:117], 0, s[0:1]
	v_add_co_u32_e32 v116, vcc, s28, v116
	v_readlane_b32 s8, v255, 48
	s_nop 0
	v_addc_co_u32_e32 v117, vcc, 0, v117, vcc
	global_load_dwordx4 v[116:119], v[116:117], off
	global_load_dwordx4 v[124:127], v[114:115], off offset:1024
	global_load_dwordx4 v[128:131], v[114:115], off offset:2048
	global_load_dwordx4 v[132:135], v[114:115], off offset:3072
	v_readlane_b32 s9, v255, 49
	s_mov_b64 s[0:1], -1
	s_and_b64 vcc, exec, s[8:9]
	v_lshlrev_b32_e32 v11, 2, v14
	s_waitcnt vmcnt(0)
	v_pk_fma_f32 v[74:75], v[4:5], v[118:119], v[74:75]
	v_pk_fma_f32 v[76:77], v[2:3], v[116:117], v[76:77]
	v_lshlrev_b32_e32 v2, 16, v106
	v_and_b32_e32 v3, 0xffff0000, v106
	v_lshlrev_b32_e32 v4, 16, v108
	v_and_b32_e32 v5, 0xffff0000, v108
	v_pk_add_f32 v[2:3], v[2:3], v[4:5]
	v_lshlrev_b32_e32 v4, 16, v110
	v_and_b32_e32 v5, 0xffff0000, v110
	v_lshlrev_b32_e32 v116, 16, v112
	v_and_b32_e32 v117, 0xffff0000, v112
	v_pk_add_f32 v[4:5], v[4:5], v[116:117]
	v_lshlrev_b32_e32 v106, 16, v113
	v_pk_add_f32 v[116:117], v[2:3], v[4:5]
	v_lshlrev_b32_e32 v2, 16, v107
	v_and_b32_e32 v3, 0xffff0000, v107
	v_lshlrev_b32_e32 v4, 16, v109
	v_and_b32_e32 v5, 0xffff0000, v109
	v_pk_add_f32 v[2:3], v[2:3], v[4:5]
	v_lshlrev_b32_e32 v4, 16, v111
	v_and_b32_e32 v5, 0xffff0000, v111
	v_and_b32_e32 v107, 0xffff0000, v113
	v_pk_add_f32 v[4:5], v[4:5], v[106:107]
	s_nop 0
	v_pk_add_f32 v[106:107], v[2:3], v[4:5]
	v_mov_b64_e32 v[2:3], v[124:125]
	v_mov_b64_e32 v[4:5], v[126:127]
	s_nop 0
	v_pk_fma_f32 v[78:79], v[106:107], v[4:5], v[78:79]
	v_pk_fma_f32 v[80:81], v[116:117], v[2:3], v[80:81]
	v_lshlrev_b32_e32 v2, 16, v104
	v_and_b32_e32 v3, 0xffff0000, v104
	v_lshlrev_b32_e32 v4, 16, v102
	v_and_b32_e32 v5, 0xffff0000, v102
	v_pk_add_f32 v[2:3], v[2:3], v[4:5]
	v_lshlrev_b32_e32 v4, 16, v100
	v_and_b32_e32 v5, 0xffff0000, v100
	v_lshlrev_b32_e32 v106, 16, v90
	v_and_b32_e32 v107, 0xffff0000, v90
	v_pk_add_f32 v[4:5], v[4:5], v[106:107]
	v_lshlrev_b32_e32 v90, 16, v91
	v_pk_add_f32 v[106:107], v[2:3], v[4:5]
	v_lshlrev_b32_e32 v2, 16, v105
	v_and_b32_e32 v3, 0xffff0000, v105
	v_lshlrev_b32_e32 v4, 16, v103
	v_and_b32_e32 v5, 0xffff0000, v103
	v_pk_add_f32 v[2:3], v[2:3], v[4:5]
	v_lshlrev_b32_e32 v4, 16, v101
	v_and_b32_e32 v5, 0xffff0000, v101
	v_and_b32_e32 v91, 0xffff0000, v91
	v_pk_add_f32 v[4:5], v[4:5], v[90:91]
	s_nop 0
	v_pk_add_f32 v[90:91], v[2:3], v[4:5]
	v_mov_b64_e32 v[2:3], v[128:129]
	v_mov_b64_e32 v[4:5], v[130:131]
	s_nop 0
	v_pk_fma_f32 v[82:83], v[90:91], v[4:5], v[82:83]
	v_pk_fma_f32 v[84:85], v[106:107], v[2:3], v[84:85]
	v_lshlrev_b32_e32 v2, 16, v98
	v_and_b32_e32 v3, 0xffff0000, v98
	v_lshlrev_b32_e32 v4, 16, v96
	v_and_b32_e32 v5, 0xffff0000, v96
	v_pk_add_f32 v[2:3], v[2:3], v[4:5]
	v_lshlrev_b32_e32 v4, 16, v94
	v_and_b32_e32 v5, 0xffff0000, v94
	v_lshlrev_b32_e32 v90, 16, v92
	v_and_b32_e32 v91, 0xffff0000, v92
	v_pk_add_f32 v[4:5], v[4:5], v[90:91]
	v_lshlrev_b32_e32 v92, 16, v93
	v_pk_add_f32 v[90:91], v[2:3], v[4:5]
	v_lshlrev_b32_e32 v2, 16, v99
	v_and_b32_e32 v3, 0xffff0000, v99
	v_lshlrev_b32_e32 v4, 16, v97
	v_and_b32_e32 v5, 0xffff0000, v97
	v_pk_add_f32 v[2:3], v[2:3], v[4:5]
	v_lshlrev_b32_e32 v4, 16, v95
	v_and_b32_e32 v5, 0xffff0000, v95
	v_and_b32_e32 v93, 0xffff0000, v93
	v_pk_add_f32 v[4:5], v[4:5], v[92:93]
	v_pk_mul_f32 v[96:97], v[76:77], v[76:77]
	v_pk_add_f32 v[92:93], v[2:3], v[4:5]
	v_mov_b64_e32 v[2:3], v[132:133]
	v_mov_b64_e32 v[4:5], v[134:135]
	v_pk_mul_f32 v[94:95], v[80:81], v[80:81]
	s_nop 0
	v_pk_fma_f32 v[88:89], v[92:93], v[4:5], v[88:89]
	v_pk_fma_f32 v[86:87], v[90:91], v[2:3], v[86:87]
	v_mul_f32_e32 v4, v88, v88
	v_mul_f32_e32 v92, v86, v86
	v_mul_f32_e32 v90, v87, v87
	v_mul_f32_e32 v2, v89, v89
	s_cbranch_vccz .LBB0_1733
	s_mov_b64 s[0:1], 0x178000
	v_lshl_add_u64 v[98:99], v[30:31], 0, s[0:1]
	s_mov_b64 s[0:1], 0x178200
	v_cvt_pk_bf16_f32 v106, v76, v77
	v_cvt_pk_bf16_f32 v107, v74, v75
	v_lshl_add_u64 v[100:101], v[30:31], 0, s[0:1]
	s_mov_b64 s[0:1], 0x178400
	global_store_dwordx2 v[98:99], v[106:107], off
	v_cvt_pk_bf16_f32 v98, v80, v81
	v_cvt_pk_bf16_f32 v99, v78, v79
	v_lshl_add_u64 v[102:103], v[30:31], 0, s[0:1]
	s_mov_b64 s[0:1], 0x178600
	global_store_dwordx2 v[100:101], v[98:99], off
	v_cvt_pk_bf16_f32 v98, v84, v85
	v_cvt_pk_bf16_f32 v99, v82, v83
	v_lshl_add_u64 v[104:105], v[30:31], 0, s[0:1]
	global_store_dwordx2 v[102:103], v[98:99], off
	v_cvt_pk_bf16_f32 v98, v86, v87
	v_cvt_pk_bf16_f32 v99, v88, v89
	global_store_dwordx2 v[104:105], v[98:99], off
	v_pk_mul_f32 v[98:99], v[74:75], v[74:75]
	v_mov_b32_e32 v100, v96
	v_mov_b32_e32 v101, v99
	v_pk_mov_b32 v[98:99], v[96:97], v[98:99] op_sel:[1,0]
	s_add_u32 s8, s22, s10
	v_pk_add_f32 v[98:99], v[98:99], v[100:101]
	v_mov_b32_e32 v100, v94
	v_pk_add_f32 v[110:111], v[98:99], v[98:99] op_sel_hi:[0,1]
	v_pk_mul_f32 v[98:99], v[78:79], v[78:79]
	s_addc_u32 s9, s23, s3
	v_mov_b32_e32 v101, v99
	v_pk_mov_b32 v[98:99], v[94:95], v[98:99] op_sel:[1,0]
	s_add_u32 s10, s8, 0x1000
	v_pk_add_f32 v[98:99], v[98:99], v[100:101]
	s_addc_u32 s11, s9, 0
	v_pk_add_f32 v[112:113], v[98:99], v[98:99] op_sel_hi:[0,1]
	v_mul_f32_e32 v98, v84, v84
	v_pk_fma_f32 v[114:115], v[84:85], v[84:85], v[98:99] op_sel_hi:[1,1,0]
	v_mul_f32_e32 v98, v82, v82
	v_pk_fma_f32 v[116:117], v[82:83], v[82:83], v[98:99] op_sel_hi:[1,1,0]
	global_load_dwordx4 v[98:101], v[16:17], off
	global_load_dwordx4 v[102:105], v34, s[8:9]
	global_load_dwordx4 v[106:109], v34, s[10:11]
	global_load_dwordx4 v[136:139], v[18:19], off
	global_load_dwordx4 v[140:143], v15, s[10:11]
	global_load_dwordx4 v[144:147], v34, s[8:9] offset:1024
	global_load_dwordx4 v[148:151], v[20:21], off
	global_load_dwordx4 v[152:155], v13, s[10:11]
	global_load_dwordx4 v[156:159], v34, s[8:9] offset:2048
	global_load_dwordx4 v[172:175], v[22:23], off
	global_load_dwordx4 v[176:179], v11, s[10:11]
	global_load_dwordx4 v[180:183], v34, s[8:9] offset:3072
	v_mov_b32_e32 v5, v111
	v_mov_b32_e32 v3, v113
	v_mov_b32_e32 v93, v115
	v_mov_b32_e32 v91, v117
	v_pk_add_f32 v[110:111], v[4:5], v[2:3]
	v_and_b32_e32 v5, 64, v203
	v_pk_add_f32 v[114:115], v[92:93], v[90:91]
	v_add_u32_e32 v5, 64, v5
	v_xor_b32_e32 v91, 1, v203
	v_cmp_lt_i32_e32 vcc, v91, v5
	v_pk_add_f32 v[110:111], v[114:115], v[110:111]
	s_mov_b32 s0, 0x4578000
	v_cndmask_b32_e32 v91, v203, v91, vcc
	v_add_f32_e32 v3, v110, v111
	v_lshlrev_b32_e32 v91, 2, v91
	s_nop 1
	v_mov_b32_dpp v91, v3 quad_perm:[1,0,3,2] row_mask:0xf bank_mask:0xf
	s_waitcnt lgkmcnt(0)
	v_add_f32_e32 v3, v3, v91
	v_xor_b32_e32 v91, 2, v203
	v_cmp_lt_i32_e32 vcc, v91, v5
	s_waitcnt vmcnt(0)
	v_pk_add_f32 v[108:109], v[108:109], 1.0 op_sel_hi:[1,0]
	v_cndmask_b32_e32 v91, v203, v91, vcc
	v_lshlrev_b32_e32 v91, 2, v91
	s_nop 1
	v_mov_b32_dpp v91, v3 quad_perm:[2,3,0,1] row_mask:0xf bank_mask:0xf
	v_pk_add_f32 v[106:107], v[106:107], 1.0 op_sel_hi:[1,0]
	s_waitcnt lgkmcnt(0)
	v_add_f32_e32 v3, v3, v91
	v_xor_b32_e32 v91, 4, v203
	v_cmp_lt_i32_e32 vcc, v91, v5
	s_nop 1
	v_cndmask_b32_e32 v91, v203, v91, vcc
	v_lshlrev_b32_e32 v91, 2, v91
	s_nop 1
	v_mov_b32_dpp v91, v3 row_half_mirror row_mask:0xf bank_mask:0xf
	s_waitcnt lgkmcnt(0)
	v_add_f32_e32 v3, v3, v91
	v_xor_b32_e32 v91, 8, v203
	v_cmp_lt_i32_e32 vcc, v91, v5
	s_nop 1
	v_cndmask_b32_e32 v91, v203, v91, vcc
	v_lshlrev_b32_e32 v91, 2, v91
	s_nop 1
	v_mov_b32_dpp v91, v3 row_mirror row_mask:0xf bank_mask:0xf
	s_waitcnt lgkmcnt(0)
	v_add_f32_e32 v3, v3, v91
	v_xor_b32_e32 v91, 16, v203
	v_cmp_lt_i32_e32 vcc, v91, v5
	s_nop 1
	v_cndmask_b32_e32 v91, v203, v91, vcc
	v_lshlrev_b32_e32 v91, 2, v91
	v_mov_b32_e32 v91, v3
	s_nop 1
	v_permlane16_swap_b32_e32 v91, v3
	s_waitcnt lgkmcnt(0)
	v_add_f32_e32 v3, v3, v91
	v_xor_b32_e32 v91, 32, v203
	v_cmp_lt_i32_e32 vcc, v91, v5
	s_nop 1
	v_cndmask_b32_e32 v5, v203, v91, vcc
	v_lshlrev_b32_e32 v5, 2, v5
	v_mov_b32_e32 v5, v3
	s_nop 1
	v_permlane32_swap_b32_e32 v5, v3
	s_waitcnt lgkmcnt(0)
	v_add_f32_e32 v3, v3, v5
	v_fmamk_f32 v3, v3, 0x3a800000, v165
	v_rsq_f32_e32 v110, v3
	s_nop 0
	v_pk_mul_f32 v[112:113], v[74:75], v[110:111] op_sel_hi:[1,0]
	v_pk_mul_f32 v[114:115], v[76:77], v[110:111] op_sel_hi:[1,0]
	v_pk_mul_f32 v[100:101], v[100:101], v[112:113]
	v_pk_mul_f32 v[98:99], v[98:99], v[114:115]
	v_pk_fma_f32 v[100:101], v[108:109], v[100:101], v[104:105]
	v_pk_fma_f32 v[98:99], v[106:107], v[98:99], v[102:103]
	v_add_co_u32_e32 v112, vcc, s0, v30
	v_cvt_pk_bf16_f32 v98, v98, v99
	v_cvt_pk_bf16_f32 v99, v100, v101
	v_addc_co_u32_e32 v113, vcc, 0, v31, vcc
	global_store_dwordx2 v[112:113], v[98:99], off
	v_mov_b64_e32 v[98:99], v[136:137]
	v_mov_b64_e32 v[100:101], v[138:139]
	v_mov_b64_e32 v[102:103], v[140:141]
	v_mov_b64_e32 v[104:105], v[142:143]
	v_mov_b64_e32 v[106:107], v[144:145]
	v_mov_b64_e32 v[108:109], v[146:147]
	s_nop 0
	s_nop 0
	s_nop 0
	v_pk_mul_f32 v[114:115], v[78:79], v[110:111] op_sel_hi:[1,0]
	v_pk_mul_f32 v[116:117], v[80:81], v[110:111] op_sel_hi:[1,0]
	s_mov_b64 s[0:1], 0
	s_nop 0
	v_pk_mul_f32 v[98:99], v[98:99], v[116:117]
	v_pk_mul_f32 v[100:101], v[100:101], v[114:115]
	s_nop 0
	v_pk_add_f32 v[104:105], v[104:105], 1.0 op_sel_hi:[1,0]
	v_pk_add_f32 v[102:103], v[102:103], 1.0 op_sel_hi:[1,0]
	s_nop 0
	v_pk_fma_f32 v[100:101], v[104:105], v[100:101], v[108:109]
	v_pk_fma_f32 v[98:99], v[102:103], v[98:99], v[106:107]
	v_pk_mul_f32 v[114:115], v[82:83], v[110:111] op_sel_hi:[1,0]
	v_cvt_pk_bf16_f32 v98, v98, v99
	v_cvt_pk_bf16_f32 v99, v100, v101
	global_store_dwordx2 v[112:113], v[98:99], off offset:512
	v_mov_b64_e32 v[98:99], v[148:149]
	v_mov_b64_e32 v[100:101], v[150:151]
	v_mov_b64_e32 v[102:103], v[152:153]
	v_mov_b64_e32 v[104:105], v[154:155]
	v_mov_b64_e32 v[106:107], v[156:157]
	v_mov_b64_e32 v[108:109], v[158:159]
	s_nop 0
	s_nop 0
	s_nop 0
	v_pk_mul_f32 v[116:117], v[84:85], v[110:111] op_sel_hi:[1,0]
	s_nop 0
	v_pk_mul_f32 v[100:101], v[114:115], v[100:101]
	v_pk_mul_f32 v[98:99], v[116:117], v[98:99]
	s_nop 0
	v_pk_add_f32 v[104:105], v[104:105], 1.0 op_sel_hi:[1,0]
	v_pk_add_f32 v[102:103], v[102:103], 1.0 op_sel_hi:[1,0]
	s_nop 0
	v_pk_fma_f32 v[100:101], v[100:101], v[104:105], v[108:109]
	v_pk_fma_f32 v[98:99], v[98:99], v[102:103], v[106:107]
	v_pk_mul_f32 v[114:115], v[88:89], v[110:111] op_sel_hi:[1,0]
	v_cvt_pk_bf16_f32 v98, v98, v99
	v_cvt_pk_bf16_f32 v99, v100, v101
	global_store_dwordx2 v[112:113], v[98:99], off offset:1024
	v_mov_b64_e32 v[98:99], v[172:173]
	v_mov_b64_e32 v[100:101], v[174:175]
	v_mov_b64_e32 v[102:103], v[176:177]
	v_mov_b64_e32 v[104:105], v[178:179]
	v_mov_b64_e32 v[106:107], v[180:181]
	v_mov_b64_e32 v[108:109], v[182:183]
	s_nop 0
	s_nop 0
	s_nop 0
	v_pk_mul_f32 v[110:111], v[86:87], v[110:111] op_sel_hi:[1,0]
	s_nop 0
	v_pk_mul_f32 v[100:101], v[114:115], v[100:101]
	v_pk_mul_f32 v[98:99], v[110:111], v[98:99]
	s_nop 0
	v_pk_add_f32 v[104:105], v[104:105], 1.0 op_sel_hi:[1,0]
	v_pk_add_f32 v[102:103], v[102:103], 1.0 op_sel_hi:[1,0]
	s_nop 0
	v_pk_fma_f32 v[100:101], v[100:101], v[104:105], v[108:109]
	v_pk_fma_f32 v[98:99], v[98:99], v[102:103], v[106:107]
	s_nop 0
	v_cvt_pk_bf16_f32 v98, v98, v99
	v_cvt_pk_bf16_f32 v99, v100, v101
	global_store_dwordx2 v[112:113], v[98:99], off offset:1536
